# v66 + indexer key-tile loads at agent scope (sc1: no L1 allocation for the no-reuse tile stream)
# speedup vs baseline: 1.0017x; 1.0017x over previous
.LBB0_1226:
	s_or_b64 exec, exec, s[0:1]
	s_waitcnt lgkmcnt(0)
	s_barrier
	v_mov_b32_e32 v0, 0x20420
	ds_read_b32 v0, v0
	s_add_u32 s0, s74, 0xc800000
	s_addc_u32 s1, s75, 0
	s_add_u32 s14, s74, 0xe800000
	s_addc_u32 s15, s75, 0
	s_movk_i32 s16, 0xfff
	s_add_u32 s82, s74, 0xea00000
	s_waitcnt lgkmcnt(0)
	v_cmp_lt_u32_e32 vcc, s16, v0
	s_movk_i32 s16, 0x1000
	s_addc_u32 s83, s75, 0
	v_readfirstlane_b32 s17, v0
	v_cmp_gt_u32_e64 s[38:39], s16, v0
	s_cbranch_vccnz .LBB0_1228
	s_not_b32 s16, s17
	s_lshl_b32 s16, s16, 1
	s_lshl_b32 s31, s17, 13
	s_and_b32 s29, s16, 0x1ffc
	s_and_b32 s31, s31, 0x2000
	v_lshrrev_b32_e32 v0, 3, v235
	v_and_b32_e32 v0, 2, v0
	v_bfe_u32 v2, v235, 2, 1
	s_or_b32 s29, s29, s31
	v_and_b32_e32 v3, 3, v235
	v_lshrrev_b32_e32 v5, 1, v235
	v_or3_b32 v0, v0, v2, s29
	v_and_or_b32 v5, v5, 4, v3
	v_lshlrev_b32_e32 v0, 10, v0
	v_lshrrev_b32_e32 v4, 5, v198
	v_lshl_add_u64 v[2:3], s[0:1], 0, v[0:1]
	v_lshlrev_b32_e32 v0, 7, v5
	v_lshl_add_u64 v[2:3], v[2:3], 0, v[0:1]
	v_lshlrev_b32_e32 v0, 4, v4
	s_bfe_u32 s16, s16, 0x80005
	v_readlane_b32 s34, v253, 32
	v_lshl_add_u64 v[2:3], v[2:3], 0, v[0:1]
	v_or_b32_e32 v0, s29, v4
	v_readlane_b32 s35, v253, 33
	s_min_i32 s29, s34, s16
	s_add_i32 s34, s34, 8
	s_min_i32 s16, s34, s16
	s_lshr_b32 s31, s31, 5
	s_ashr_i32 s35, s29, 31
	s_add_u32 s34, s29, s31
	s_addc_u32 s35, s35, 0
	s_lshl_b64 s[34:35], s[34:35], 12
	s_add_u32 s34, s14, s34
	s_addc_u32 s35, s15, s35
	s_ashr_i32 s29, s16, 31
	s_add_u32 s40, s16, s31
	s_addc_u32 s41, s29, 0
	v_lshlrev_b32_e32 v0, 5, v0
	s_lshl_b64 s[40:41], s[40:41], 12
	global_load_dwordx4 v[18:21], v[2:3], off
	global_load_dwordx4 v[26:29], v[2:3], off offset:32
	global_load_dwordx4 v[30:33], v[2:3], off offset:64
	global_load_dwordx4 v[34:37], v[2:3], off offset:96
	global_load_dwordx4 v[22:25], v0, s[82:83]
	global_load_dwordx4 v[38:41], v0, s[82:83] offset:16
	global_load_dwordx4 v[42:45], v0, s[82:83] offset:64
	global_load_dwordx4 v[46:49], v0, s[82:83] offset:80
	v_lshlrev_b32_e32 v0, 4, v198
	s_add_u32 s40, s14, s40
	s_addc_u32 s41, s15, s41
	global_load_dwordx4 v[50:53], v0, s[34:35] sc1
	global_load_dwordx4 v[62:65], v0, s[34:35] offset:1024 sc1
	global_load_dwordx4 v[78:81], v0, s[40:41] sc1
	global_load_dwordx4 v[70:73], v0, s[40:41] offset:1024 sc1
	global_load_dwordx4 v[58:61], v0, s[34:35] offset:2048 sc1
	global_load_dwordx4 v[54:57], v0, s[34:35] offset:3072 sc1
	global_load_dwordx4 v[74:77], v0, s[40:41] offset:2048 sc1
	global_load_dwordx4 v[66:69], v0, s[40:41] offset:3072 sc1
	s_andn2_b64 vcc, exec, s[38:39]
	s_cbranch_vccz .LBB0_1229
	s_branch .LBB0_1988

.LBB0_1238:
	s_add_i32 s41, s29, -16
	s_min_i32 s41, s41, s1
	s_sub_i32 s40, s29, 32
	s_ashr_i32 s43, s41, 31
	s_add_u32 s42, s17, s41
	s_addc_u32 s43, 0, s43
	s_lshl_b64 s[42:43], s[42:43], 12
	s_waitcnt vmcnt(7) lgkmcnt(0)
	v_mfma_f32_32x32x16_bf16 v[2:17], v[18:21], v[50:53], 0
	v_lshl_add_u64 v[50:51], v[100:101], 0, s[42:43]
	global_load_dwordx4 v[94:97], v[50:51], off sc1
	global_load_dwordx4 v[90:93], v[50:51], off offset:1024 sc1
	global_load_dwordx4 v[86:89], v[50:51], off offset:2048 sc1
	global_load_dwordx4 v[82:85], v[50:51], off offset:3072 sc1
	s_cmp_lt_i32 s40, s1
	s_waitcnt vmcnt(10)
	v_mfma_f32_32x32x16_bf16 v[2:17], v[26:29], v[62:65], v[2:17]
	s_waitcnt vmcnt(7)
	v_mfma_f32_32x32x16_bf16 v[2:17], v[30:33], v[58:61], v[2:17]
	s_waitcnt vmcnt(6)
	v_mfma_f32_32x32x16_bf16 v[2:17], v[34:37], v[54:57], v[2:17]
	s_nop 11
	v_med3_f32 v2, v2, 0, v233
	v_med3_f32 v10, v10, 0, v233
	v_mul_f32_e32 v2, v22, v2
	v_mul_f32_e32 v10, v42, v10
	v_med3_f32 v3, v3, 0, v233
	v_fmac_f32_e32 v2, v23, v3
	v_med3_f32 v11, v11, 0, v233
	v_fmac_f32_e32 v10, v43, v11
	v_med3_f32 v3, v4, 0, v233
	v_fmac_f32_e32 v2, v24, v3
	v_med3_f32 v4, v12, 0, v233
	v_fmac_f32_e32 v10, v44, v4
	v_med3_f32 v3, v5, 0, v233
	v_fmac_f32_e32 v2, v25, v3
	v_med3_f32 v4, v13, 0, v233
	v_fmac_f32_e32 v10, v45, v4
	v_med3_f32 v3, v6, 0, v233
	v_fmac_f32_e32 v2, v38, v3
	v_med3_f32 v4, v14, 0, v233
	v_fmac_f32_e32 v10, v46, v4
	v_med3_f32 v3, v7, 0, v233
	v_fmac_f32_e32 v2, v39, v3
	v_med3_f32 v4, v15, 0, v233
	v_fmac_f32_e32 v10, v47, v4
	v_med3_f32 v3, v8, 0, v233
	v_fmac_f32_e32 v2, v40, v3
	v_med3_f32 v4, v16, 0, v233
	v_fmac_f32_e32 v10, v48, v4
	v_med3_f32 v3, v9, 0, v233
	v_fmac_f32_e32 v2, v41, v3
	v_med3_f32 v4, v17, 0, v233
	v_fmac_f32_e32 v10, v49, v4
	v_ashrrev_i32_e32 v3, 31, v2
	v_bitop3_b32 v112, v3, v2, s97 bitop3:0x36
	v_ashrrev_i32_e32 v2, 31, v10
	v_bitop3_b32 v113, v2, v10, s97 bitop3:0x36
	s_cbranch_scc1 .LBB0_1240
	v_cmp_le_i32_e32 vcc, v110, v109
	s_nop 1
	v_cndmask_b32_e32 v113, 0, v113, vcc
	v_cmp_le_i32_e32 vcc, v110, v108
	s_nop 1
	v_cndmask_b32_e32 v112, 0, v112, vcc
.LBB0_1240:
	s_add_i32 s41, s29, -8
	s_min_i32 s41, s41, s1
	s_ashr_i32 s43, s41, 31
	s_add_u32 s42, s17, s41
	s_addc_u32 s43, 0, s43
	s_lshl_b64 s[42:43], s[42:43], 12
	v_lshl_add_u64 v[54:55], v[100:101], 0, s[42:43]
	global_load_dwordx4 v[50:53], v[54:55], off sc1
	global_load_dwordx4 v[62:65], v[54:55], off offset:1024 sc1
	global_load_dwordx4 v[58:61], v[54:55], off offset:2048 sc1
	s_nop 0
	global_load_dwordx4 v[54:57], v[54:55], off offset:3072 sc1
	v_mfma_f32_32x32x16_bf16 v[2:17], v[18:21], v[78:81], 0
	s_add_i32 s40, s40, 8
	s_cmp_lt_i32 s40, s1
	ds_write_b32 v111, v112
	v_mfma_f32_32x32x16_bf16 v[2:17], v[26:29], v[70:73], v[2:17]
	v_add_u32_e32 v70, 0x10000, v111
	ds_write_b32 v70, v113
	s_waitcnt vmcnt(9)
	v_mfma_f32_32x32x16_bf16 v[2:17], v[30:33], v[74:77], v[2:17]
	s_waitcnt vmcnt(8)
	v_mfma_f32_32x32x16_bf16 v[2:17], v[34:37], v[66:69], v[2:17]
	s_nop 11
	v_med3_f32 v2, v2, 0, v233
	v_med3_f32 v10, v10, 0, v233
	v_mul_f32_e32 v2, v22, v2
	v_med3_f32 v3, v3, 0, v233
	v_mul_f32_e32 v10, v42, v10
	v_fmac_f32_e32 v2, v23, v3
	v_med3_f32 v3, v4, 0, v233
	v_med3_f32 v11, v11, 0, v233
	v_fmac_f32_e32 v10, v43, v11
	v_fmac_f32_e32 v2, v24, v3
	v_med3_f32 v3, v5, 0, v233
	v_med3_f32 v4, v12, 0, v233
	v_fmac_f32_e32 v10, v44, v4
	v_fmac_f32_e32 v2, v25, v3
	v_med3_f32 v3, v6, 0, v233
	v_med3_f32 v4, v13, 0, v233
	v_fmac_f32_e32 v10, v45, v4
	v_fmac_f32_e32 v2, v38, v3
	v_med3_f32 v3, v7, 0, v233
	v_med3_f32 v4, v14, 0, v233
	v_fmac_f32_e32 v10, v46, v4
	v_fmac_f32_e32 v2, v39, v3
	v_med3_f32 v3, v8, 0, v233
	v_med3_f32 v4, v15, 0, v233
	v_fmac_f32_e32 v10, v47, v4
	v_fmac_f32_e32 v2, v40, v3
	v_med3_f32 v3, v9, 0, v233
	v_med3_f32 v4, v16, 0, v233
	v_fmac_f32_e32 v10, v48, v4
	v_fmac_f32_e32 v2, v41, v3
	v_med3_f32 v4, v17, 0, v233
	v_ashrrev_i32_e32 v3, 31, v2
	v_fmac_f32_e32 v10, v49, v4
	v_bitop3_b32 v2, v3, v2, s97 bitop3:0x36
	s_nop 0
	v_ashrrev_i32_e32 v3, 31, v10
	v_bitop3_b32 v3, v3, v10, s97 bitop3:0x36
	s_cbranch_scc1 .LBB0_1242
	v_add_u32_e32 v4, 0x100, v110
	v_cmp_le_i32_e32 vcc, v4, v109
	s_nop 1
	v_cndmask_b32_e32 v3, 0, v3, vcc
	v_cmp_le_i32_e32 vcc, v4, v108
	s_nop 1
	v_cndmask_b32_e32 v2, 0, v2, vcc

.LBB0_1244:
	s_min_i32 s41, s29, s1
	s_ashr_i32 s43, s41, 31
	s_add_u32 s42, s17, s41
	s_addc_u32 s43, 0, s43
	s_lshl_b64 s[42:43], s[42:43], 12
	v_lshl_add_u64 v[66:67], v[100:101], 0, s[42:43]
	global_load_dwordx4 v[78:81], v[66:67], off sc1
	global_load_dwordx4 v[70:73], v[66:67], off offset:1024 sc1
	global_load_dwordx4 v[74:77], v[66:67], off offset:2048 sc1
	s_nop 0
	global_load_dwordx4 v[66:69], v[66:67], off offset:3072 sc1
	s_waitcnt vmcnt(11)
	v_mfma_f32_32x32x16_bf16 v[2:17], v[18:21], v[94:97], 0
	s_add_i32 s40, s40, 8
	s_cmp_lt_i32 s40, s1
	s_waitcnt vmcnt(10)
	v_mfma_f32_32x32x16_bf16 v[2:17], v[26:29], v[90:93], v[2:17]
	s_waitcnt vmcnt(9)
	v_mfma_f32_32x32x16_bf16 v[2:17], v[30:33], v[86:89], v[2:17]
	s_waitcnt vmcnt(8)
	v_mfma_f32_32x32x16_bf16 v[2:17], v[34:37], v[82:85], v[2:17]
	s_nop 11
	v_med3_f32 v2, v2, 0, v233
	v_med3_f32 v10, v10, 0, v233
	v_mul_f32_e32 v2, v22, v2
	v_med3_f32 v3, v3, 0, v233
	v_mul_f32_e32 v10, v42, v10
	v_fmac_f32_e32 v2, v23, v3
	v_med3_f32 v3, v4, 0, v233
	v_med3_f32 v11, v11, 0, v233
	v_fmac_f32_e32 v10, v43, v11
	v_fmac_f32_e32 v2, v24, v3
	v_med3_f32 v3, v5, 0, v233
	v_med3_f32 v4, v12, 0, v233
	v_fmac_f32_e32 v10, v44, v4
	v_fmac_f32_e32 v2, v25, v3
	v_med3_f32 v3, v6, 0, v233
	v_med3_f32 v4, v13, 0, v233
	v_fmac_f32_e32 v10, v45, v4
	v_fmac_f32_e32 v2, v38, v3
	v_med3_f32 v3, v7, 0, v233
	v_med3_f32 v4, v14, 0, v233
	v_fmac_f32_e32 v10, v46, v4
	v_fmac_f32_e32 v2, v39, v3
	v_med3_f32 v3, v8, 0, v233
	v_med3_f32 v4, v15, 0, v233
	v_fmac_f32_e32 v10, v47, v4
	v_fmac_f32_e32 v2, v40, v3
	v_med3_f32 v3, v9, 0, v233
	v_med3_f32 v4, v16, 0, v233
	v_fmac_f32_e32 v10, v48, v4
	v_fmac_f32_e32 v2, v41, v3
	v_med3_f32 v4, v17, 0, v233
	v_ashrrev_i32_e32 v3, 31, v2
	v_fmac_f32_e32 v10, v49, v4
	v_bitop3_b32 v2, v3, v2, s97 bitop3:0x36
	s_nop 0
	v_ashrrev_i32_e32 v3, 31, v10
	v_bitop3_b32 v3, v3, v10, s97 bitop3:0x36
	s_cbranch_scc1 .LBB0_1246
	v_add_u32_e32 v4, 0x200, v110
	v_cmp_le_i32_e32 vcc, v4, v109
	s_nop 1
	v_cndmask_b32_e32 v3, 0, v3, vcc
	v_cmp_le_i32_e32 vcc, v4, v108
	s_nop 1
	v_cndmask_b32_e32 v2, 0, v2, vcc

.LBB0_1252:
	s_or_b64 exec, exec, s[40:41]
	s_lshl_b32 s17, s17, 2
	s_or_b32 s17, s17, 0x20420
	s_waitcnt lgkmcnt(0)
	s_barrier
	v_mov_b32_e32 v0, s17
	ds_read_b32 v0, v0
	s_movk_i32 s29, 0xfff
	s_waitcnt lgkmcnt(0)
	v_cmp_lt_u32_e64 s[40:41], s29, v0
	v_readfirstlane_b32 s17, v0
	s_and_b64 vcc, exec, s[40:41]
	s_cbranch_vccnz .LBB0_1256
	s_not_b32 s29, s17
	s_lshl_b32 s29, s29, 1
	s_lshl_b32 s43, s17, 13
	s_and_b32 s42, s29, 0x1ffc
	s_and_b32 s43, s43, 0x2000
	s_or_b32 s42, s42, s43
	v_or_b32_e32 v0, s42, v143
	v_lshlrev_b32_e32 v0, 10, v0
	s_bfe_u32 s29, s29, 0x80005
	v_readlane_b32 s44, v253, 32
	v_lshl_add_u64 v[2:3], v[102:103], 0, v[0:1]
	v_or_b32_e32 v0, s42, v140
	s_min_i32 s42, s44, s29
	v_readlane_b32 s44, v253, 31
	s_min_i32 s29, s44, s29
	s_lshr_b32 s44, s43, 5
	s_ashr_i32 s43, s42, 31
	s_add_u32 s42, s42, s44
	s_addc_u32 s43, s43, 0
	s_lshl_b64 s[42:43], s[42:43], 12
	global_load_dwordx4 v[18:21], v[2:3], off
	global_load_dwordx4 v[26:29], v[2:3], off offset:32
	global_load_dwordx4 v[30:33], v[2:3], off offset:64
	global_load_dwordx4 v[34:37], v[2:3], off offset:96
	v_lshl_add_u64 v[2:3], v[100:101], 0, s[42:43]
	s_ashr_i32 s43, s29, 31
	s_add_u32 s42, s29, s44
	s_addc_u32 s43, s43, 0
	v_lshlrev_b32_e32 v0, 5, v0
	s_lshl_b64 s[42:43], s[42:43], 12
	global_load_dwordx4 v[22:25], v0, s[82:83]
	global_load_dwordx4 v[38:41], v0, s[82:83] offset:16
	global_load_dwordx4 v[42:45], v0, s[82:83] offset:64
	global_load_dwordx4 v[46:49], v0, s[82:83] offset:80
	v_lshl_add_u64 v[4:5], v[100:101], 0, s[42:43]
	global_load_dwordx4 v[50:53], v[2:3], off sc1
	global_load_dwordx4 v[62:65], v[2:3], off offset:1024 sc1
	global_load_dwordx4 v[78:81], v[4:5], off sc1
	global_load_dwordx4 v[70:73], v[4:5], off offset:1024 sc1
	global_load_dwordx4 v[58:61], v[2:3], off offset:2048 sc1
	global_load_dwordx4 v[54:57], v[2:3], off offset:3072 sc1
	global_load_dwordx4 v[74:77], v[4:5], off offset:2048 sc1
	global_load_dwordx4 v[66:69], v[4:5], off offset:3072 sc1
	v_readlane_b32 s45, v253, 33
	s_cmpk_lt_u32 s34, 0x100
	v_mov_b32_e32 v149, 1
	s_cbranch_scc0 .LBB0_1257
